# barrier B (and prologue barrier 2) wait only for the K/V LDS writes (lgkmcnt(8)/(4)); Q-fragment reads waited at their consumer MFMAs
# speedup vs baseline: 1.0100x; 1.0100x over previous
_Z7k_fusedPKDF16_S0_S0_S0_PKfS2_S2_Pf:
	v_lshrrev_b32_e32 v222, 6, v0
	v_and_b32_e32 v1, 63, v0
	s_load_dwordx8 s[24:31], s[0:1], 0x8
	s_load_dwordx4 s[36:39], s[0:1], 0x28
	v_lshlrev_b32_e32 v4, 2, v222
	v_lshlrev_b32_e32 v5, 3, v1
	v_lshl_or_b32 v2, v222, 11, v5
	v_lshlrev_b32_e32 v224, 12, v222
	v_or_b32_e32 v6, 1, v4
	v_lshlrev_b32_e32 v223, 1, v2
	v_readfirstlane_b32 s3, v224
	v_lshl_or_b32 v2, v6, 9, v5
	v_lshlrev_b32_e32 v225, 10, v6
	v_mov_b32_e32 v211, 0
	s_mov_b32 m0, s3
	v_lshlrev_b32_e32 v210, 1, v2
	v_readfirstlane_b32 s3, v225
	s_waitcnt lgkmcnt(0)
	global_load_lds_dwordx4 v223, s[24:25]
	v_lshl_add_u64 v[2:3], s[24:25], 0, v[210:211]
	s_mov_b32 m0, s3
	v_or_b32_e32 v6, 2, v4
	global_load_lds_dwordx4 v[2:3], off
	v_lshl_or_b32 v2, v6, 9, v5
	v_lshlrev_b32_e32 v212, 1, v2
	v_mov_b32_e32 v213, v211
	v_lshl_add_u64 v[2:3], s[24:25], 0, v[212:213]
	v_lshlrev_b32_e32 v213, 10, v6
	v_or_b32_e32 v4, 3, v4
	v_readfirstlane_b32 s3, v213
	s_mov_b32 m0, s3
	v_mov_b32_e32 v215, v211
	global_load_lds_dwordx4 v[2:3], off
	v_lshl_or_b32 v2, v4, 9, v5
	v_lshlrev_b32_e32 v214, 1, v2
	v_lshl_add_u64 v[2:3], s[24:25], 0, v[214:215]
	v_lshlrev_b32_e32 v215, 10, v4
	s_nop 0
	v_readfirstlane_b32 s3, v215
	s_mov_b32 m0, s3
	s_movk_i32 s3, 0xff
	global_load_lds_dwordx4 v[2:3], off
	v_and_b32_e32 v2, 0x7f, v0
	v_lshlrev_b32_e32 v2, 2, v2
	global_load_dword v4, v2, s[36:37]
	global_load_dword v5, v2, s[38:39]
	s_lshl_b32 s3, s2, 8
	s_load_dwordx2 s[4:5], s[0:1], 0x0
	v_and_b32_e32 v6, 0xff, v0
	v_or_b32_e32 v6, s3, v6
	v_ashrrev_i32_e32 v7, 31, v6
	v_lshl_add_u64 v[6:7], v[6:7], 2, s[30:31]
	global_load_dword v244, v[6:7], off
	v_mov_b32_e32 v208, s3
	v_lshl_or_b32 v2, s2, 3, v222
	v_ashrrev_i32_e32 v3, 31, v2
	v_lshlrev_b64 v[2:3], 13, v[2:3]
	s_waitcnt lgkmcnt(0)
	v_lshl_add_u64 v[6:7], s[4:5], 0, v[2:3]
	v_mov_b32_e32 v2, 0
	v_lshlrev_b32_e32 v206, 4, v1
	v_mov_b32_e32 v207, v2
	v_lshl_add_u64 v[6:7], v[6:7], 0, v[206:207]
	v_lshlrev_b32_e32 v211, 13, v222
	v_ashrrev_i32_e32 v209, 31, v208
	v_lshl_add_u64 v[8:9], v[208:209], 2, s[30:31]
	v_or_b32_e32 v3, v211, v206
	v_lshl_add_u64 v[8:9], v[8:9], 0, v[206:207]
	global_load_dwordx4 v[68:71], v[8:9], off
	global_load_dwordx4 v[130:133], v[6:7], off
	global_load_dwordx4 v[134:137], v[6:7], off offset:1024
	global_load_dwordx4 v[138:141], v[6:7], off offset:2048
	global_load_dwordx4 v[142:145], v[6:7], off offset:3072
	s_movk_i32 s33, 0x1000
	v_add_co_u32_e32 v14, vcc, s33, v6
	s_nop 1
	v_addc_co_u32_e32 v15, vcc, 0, v7, vcc
	global_load_dwordx4 v[146:149], v[14:15], off
	global_load_dwordx4 v[150:153], v[14:15], off offset:1024
	global_load_dwordx4 v[154:157], v[14:15], off offset:2048
	global_load_dwordx4 v[158:161], v[14:15], off offset:3072
	v_lshlrev_b32_e32 v10, 1, v3
	global_load_dwordx4 v[186:189], v10, s[28:29] offset:16
	global_load_dwordx4 v[190:193], v10, s[28:29]
	global_load_dwordx4 v[178:181], v10, s[28:29] offset:2064
	global_load_dwordx4 v[182:185], v10, s[28:29] offset:2048
	v_mov_b32_e32 v11, v2
	v_lshl_add_u64 v[8:9], s[28:29], 0, v[10:11]
	v_add_co_u32_e32 v12, vcc, s33, v8
	s_mov_b64 s[34:35], 0x1000
	s_nop 0
	v_addc_co_u32_e32 v13, vcc, 0, v9, vcc
	s_mov_b64 s[40:41], 0x1800
	v_lshl_add_u64 v[10:11], v[8:9], 0, s[34:35]
	v_lshl_add_u64 v[8:9], v[8:9], 0, s[40:41]
	global_load_dwordx4 v[170:173], v[12:13], off
	global_load_dwordx4 v[174:177], v[10:11], off offset:16
	global_load_dwordx4 v[162:165], v[12:13], off offset:2048
	global_load_dwordx4 v[166:169], v[8:9], off offset:16
	s_waitcnt vmcnt(17)
	v_cmp_gt_u32_e32 vcc, 0x100, v0
	s_and_saveexec_b64 s[4:5], vcc
	v_lshlrev_b32_e32 v12, 4, v0
	v_and_b32_e32 v13, 0xe3, v0
	v_lshlrev_b32_e32 v14, 1, v0
	v_and_b32_e32 v12, 64, v12
	s_mov_b32 s8, 0x20000
	v_and_b32_e32 v14, 48, v14
	v_lshl_or_b32 v13, v13, 2, v12
	v_or3_b32 v13, v13, v14, s8
	v_add_f32_e32 v12, -1.0, v244
	v_mul_f32_e32 v12, 0x47000000, v12
	v_mul_f32_e32 v12, 0x3fb8aa3b, v12
	ds_write_b32 v13, v12
	s_or_b64 exec, exec, s[4:5]
	s_waitcnt lgkmcnt(0)
	s_barrier
	ds_read_b128 v[4:7], v206 offset:8192
	ds_read_b128 v[72:75], v206 offset:9216
	s_load_dwordx2 s[30:31], s[0:1], 0x38
	s_mov_b32 s0, 0x47000000
	s_mov_b32 s42, 0x3fb8aa3b
	s_mov_b32 s43, 0xff800000
	v_lshrrev_b32_e32 v96, 5, v1
	v_lshlrev_b32_e32 v97, 4, v96
	v_lshl_or_b32 v209, v222, 11, v206
	v_lshlrev_b32_e32 v1, 5, v1
	s_add_u32 s54, s24, 0x8000
	v_lshlrev_b32_e32 v207, 2, v96
	s_addc_u32 s55, s25, 0
	v_or_b32_e32 v227, 0x10000, v3
	s_mov_b32 s56, 0xc1d00000
	s_mov_b64 s[44:45], 0x20000
	s_mov_b64 s[46:47], 0x20800
	s_mov_b64 s[48:49], 0x21000
	s_mov_b32 s57, 0x21000
	s_mov_b64 s[50:51], 0x21800
	v_mov_b32_e32 v194, 0x3c003c00
	s_waitcnt lgkmcnt(0)
	s_waitcnt vmcnt(15)
	v_mfma_f32_32x32x16_f16 v[36:51], v[4:7], v[130:133], 0
	ds_read_b128 v[4:7], v206
	ds_read_b128 v[76:79], v206 offset:1024
	ds_read_b128 v[20:23], v206 offset:24576
	ds_read_b128 v[80:83], v206 offset:25600
	ds_read_b128 v[52:55], v206 offset:16384
	ds_read_b128 v[84:87], v206 offset:17408
	v_max_f32_e32 v71, v71, v71
	s_waitcnt lgkmcnt(1)
	v_mfma_f32_32x32x16_f16 v[52:67], v[130:133], v[52:55], 0
	v_max_f32_e32 v70, v70, v70
	v_max_f32_e32 v70, v70, v71
	s_waitcnt vmcnt(14)
	v_mfma_f32_32x32x16_f16 v[36:51], v[72:75], v[134:137], v[36:51]
	s_waitcnt lgkmcnt(0)
	v_mfma_f32_32x32x16_f16 v[52:67], v[134:137], v[84:87], v[52:67]
	ds_read_b128 v[72:75], v206 offset:10240
	ds_read_b128 v[84:87], v206 offset:11264
	s_waitcnt lgkmcnt(1)
	s_waitcnt vmcnt(13)
	v_mfma_f32_32x32x16_f16 v[36:51], v[72:75], v[138:141], v[36:51]
	ds_read_b128 v[72:75], v206 offset:18432
	ds_read_b128 v[88:91], v206 offset:19456
	s_waitcnt lgkmcnt(1)
	v_mfma_f32_32x32x16_f16 v[52:67], v[138:141], v[72:75], v[52:67]
	ds_read_b128 v[72:75], v206 offset:12288
	s_waitcnt vmcnt(12)
	v_mfma_f32_32x32x16_f16 v[36:51], v[84:87], v[142:145], v[36:51]
	v_mbcnt_lo_u32_b32 v84, -1, 0
	v_mbcnt_hi_u32_b32 v92, -1, v84
	ds_read_b128 v[84:87], v206 offset:13312
	v_xor_b32_e32 v93, 1, v92
	v_xor_b32_e32 v94, 2, v92
	v_xor_b32_e32 v95, 4, v92
	s_waitcnt lgkmcnt(2)
	v_mfma_f32_32x32x16_f16 v[52:67], v[142:145], v[88:91], v[52:67]
	v_and_b32_e32 v88, 64, v92
	v_add_u32_e32 v98, 64, v88
	v_cmp_lt_i32_e32 vcc, v93, v98
	ds_read_b128 v[88:91], v206 offset:21504
	s_waitcnt lgkmcnt(2)
	s_waitcnt vmcnt(11)
	v_mfma_f32_32x32x16_f16 v[36:51], v[72:75], v[146:149], v[36:51]
	ds_read_b128 v[72:75], v206 offset:20480
	s_waitcnt lgkmcnt(0)
	v_mfma_f32_32x32x16_f16 v[52:67], v[146:149], v[72:75], v[52:67]
	v_cndmask_b32_e32 v72, v92, v93, vcc
	v_lshlrev_b32_e32 v72, 2, v72
	v_max3_f32 v73, v68, v69, v70
	ds_bpermute_b32 v72, v72, v73
	v_cmp_lt_i32_e32 vcc, v94, v98
	s_waitcnt lgkmcnt(0)
	v_max_f32_e32 v72, v72, v72
	v_cndmask_b32_e32 v68, v92, v94, vcc
	v_lshlrev_b32_e32 v74, 2, v68
	ds_read_b128 v[68:71], v206 offset:14336
	s_waitcnt vmcnt(10)
	v_mfma_f32_32x32x16_f16 v[36:51], v[84:87], v[150:153], v[36:51]
	v_max_f32_e32 v84, v73, v72
	ds_bpermute_b32 v85, v74, v84
	v_cmp_lt_i32_e32 vcc, v95, v98
	s_waitcnt lgkmcnt(0)
	v_max_f32_e32 v85, v85, v85
	v_mfma_f32_32x32x16_f16 v[52:67], v[150:153], v[88:91], v[52:67]
	v_cndmask_b32_e32 v72, v92, v95, vcc
	v_lshlrev_b32_e32 v86, 2, v72
	v_max_f32_e32 v92, v84, v85
	ds_read_b128 v[72:75], v206 offset:15360
	ds_bpermute_b32 v93, v86, v92
	s_waitcnt lgkmcnt(0)
	v_max_f32_e32 v93, v93, v93
	s_waitcnt vmcnt(9)
	v_mfma_f32_32x32x16_f16 v[36:51], v[68:71], v[154:157], v[36:51]
	ds_read_b128 v[68:71], v206 offset:22528
	ds_read_b128 v[84:87], v206 offset:23552
	v_max_f32_e32 v92, v92, v93
	global_load_dwordx4 v[88:91], v97, s[36:37]
	v_readlane_b32 s3, v92, 0
	v_readlane_b32 s2, v92, 8
	v_readlane_b32 s5, v92, 16
	v_readlane_b32 s4, v92, 24
	s_waitcnt lgkmcnt(1)
	v_mfma_f32_32x32x16_f16 v[52:67], v[154:157], v[68:71], v[52:67]
	v_add_f32_e64 v68, s2, -1.0
	v_add_f32_e64 v69, s3, -1.0
	v_readlane_b32 s7, v92, 32
	v_readlane_b32 s6, v92, 40
	v_add_f32_e64 v70, s4, -1.0
	v_add_f32_e64 v71, s5, -1.0
	v_pk_mul_f32 v[68:69], v[68:69], s[0:1] op_sel_hi:[1,0]
	v_readlane_b32 s9, v92, 48
	v_readlane_b32 s8, v92, 56
	v_mfma_f32_32x32x16_f16 v[20:35], v[20:23], v[130:133], 0
	v_mul_f32_e64 v70, v70, s0
	v_mul_f32_e64 v71, v71, s0
	v_mul_f32_e64 v92, v68, s42
	v_mul_f32_e64 v93, v69, s42
	v_mul_f32_e64 v94, v70, s42
	v_mul_f32_e64 v95, v71, s42
	v_max3_f32 v68, v93, s43, v92
	v_max3_f32 v68, v68, v95, v94
	s_waitcnt vmcnt(9)
	v_mfma_f32_32x32x16_f16 v[36:51], v[72:75], v[158:161], v[36:51]
	v_add_f32_e64 v72, s6, -1.0
	v_add_f32_e64 v73, s7, -1.0
	v_mul_f32_e64 v72, v72, s0
	v_mul_f32_e64 v73, v73, s0
	s_waitcnt lgkmcnt(0)
	v_mfma_f32_32x32x16_f16 v[52:67], v[158:161], v[84:87], v[52:67]
	v_mul_f32_e64 v84, v72, s42
	v_mul_f32_e64 v85, v73, s42
	v_add_f32_e64 v86, s8, -1.0
	v_add_f32_e64 v87, s9, -1.0
	v_max3_f32 v98, v68, v85, v84
	ds_read_b128 v[68:71], v206 offset:26624
	v_cvt_pk_f16_f32 v43, v42, v43
	v_cvt_pk_f16_f32 v42, v40, v41
	v_cvt_pk_f16_f32 v41, v38, v39
	v_mfma_f32_32x32x16_f16 v[20:35], v[80:83], v[134:137], v[20:35]
	v_mul_f32_e64 v80, v86, s0
	v_mul_f32_e64 v81, v87, s0
	v_cvt_pk_f16_f32 v40, v36, v37
	v_mul_f32_e64 v86, v80, s42
	v_mul_f32_e64 v87, v81, s42
	global_load_dwordx4 v[72:75], v97, s[36:37] offset:32
	v_max3_f32 v80, v98, v87, v86
	v_add_f32_e32 v98, 0xc53b8000, v80
	ds_read_b128 v[80:83], v206 offset:27648
	global_load_dwordx4 v[36:39], v97, s[36:37] offset:64
	ds_write_b128 v209, v[40:43] offset:32768
	v_cvt_pk_f16_f32 v43, v50, v51
	v_cvt_pk_f16_f32 v40, v44, v45
	v_cvt_pk_f16_f32 v44, v52, v53
	global_load_dwordx4 v[50:53], v97, s[36:37] offset:96
	s_waitcnt lgkmcnt(2)
	v_mfma_f32_32x32x16_f16 v[20:35], v[68:71], v[138:141], v[20:35]
	ds_read_b128 v[68:71], v206 offset:28672
	v_cvt_pk_f16_f32 v42, v48, v49
	v_cvt_pk_f16_f32 v41, v46, v47
	ds_write_b128 v209, v[40:43] offset:33792
	ds_read_b128 v[40:43], v206 offset:30720
	v_cvt_pk_f16_f32 v47, v58, v59
	v_cvt_pk_f16_f32 v46, v56, v57
	s_waitcnt lgkmcnt(4)
	v_mfma_f32_32x32x16_f16 v[20:35], v[80:83], v[142:145], v[20:35]
	ds_read_b128 v[80:83], v206 offset:29696
	v_cvt_pk_f16_f32 v45, v54, v55
	ds_write_b128 v209, v[44:47] offset:49152
	v_cvt_pk_f16_f32 v45, v66, v67
	ds_read_b128 v[46:49], v206 offset:31744
	v_cvt_pk_f16_f32 v44, v64, v65
	v_cmp_ge_f32_e64 s[0:1], v92, v98
	s_waitcnt lgkmcnt(5)
	v_mfma_f32_32x32x16_f16 v[20:35], v[68:71], v[146:149], v[20:35]
	v_cmp_ge_f32_e64 s[2:3], v93, v98
	v_cmp_ge_f32_e64 s[4:5], v94, v98
	v_cmp_ge_f32_e64 s[6:7], v95, v98
	v_cmp_ge_f32_e64 s[8:9], v84, v98
	v_cmp_ge_f32_e64 s[10:11], v85, v98
	v_cmp_ge_f32_e64 s[12:13], v86, v98
	v_cmp_ge_f32_e64 s[14:15], v87, v98
	v_mfma_f32_32x32x16_f16 v[4:19], v[4:7], v[130:133], 0
	s_waitcnt lgkmcnt(2)
	v_mfma_f32_32x32x16_f16 v[20:35], v[80:83], v[150:153], v[20:35]
	v_mfma_f32_32x32x16_f16 v[4:19], v[76:79], v[134:137], v[4:19]
	v_mfma_f32_32x32x16_f16 v[20:35], v[40:43], v[154:157], v[20:35]
	v_cvt_pk_f16_f32 v43, v62, v63
	v_cvt_pk_f16_f32 v42, v60, v61
	ds_write_b128 v209, v[42:45] offset:50176
	ds_read_b128 v[40:43], v206 offset:2048
	ds_read_b128 v[54:57], v206 offset:3072
	s_waitcnt lgkmcnt(1)
	v_mfma_f32_32x32x16_f16 v[4:19], v[40:43], v[138:141], v[4:19]
	s_waitcnt lgkmcnt(0)
	v_mfma_f32_32x32x16_f16 v[4:19], v[54:57], v[142:145], v[4:19]
	v_mfma_f32_32x32x16_f16 v[20:35], v[46:49], v[158:161], v[20:35]
	ds_read_b128 v[44:47], v206 offset:4096
	ds_read_b128 v[58:61], v206 offset:5120
	ds_read_b128 v[62:65], v206 offset:6144
	ds_read_b128 v[66:69], v206 offset:7168
	s_waitcnt lgkmcnt(4)
	s_barrier
	s_waitcnt vmcnt(3)
	s_nop 4
	v_add_f32_e32 v20, v20, v88
	s_waitcnt lgkmcnt(3)
	v_mfma_f32_32x32x16_f16 v[4:19], v[44:47], v[146:149], v[4:19]
	v_add_f32_e32 v21, v89, v21
	v_add_f32_e32 v22, v90, v22
	v_add_f32_e32 v23, v91, v23
	s_waitcnt vmcnt(2)
	v_add_f32_e32 v24, v24, v72
	v_add_f32_e32 v25, v73, v25
	v_add_f32_e32 v26, v74, v26
	v_add_f32_e32 v27, v75, v27
	s_waitcnt lgkmcnt(2)
	v_mfma_f32_32x32x16_f16 v[4:19], v[58:61], v[150:153], v[4:19]
	s_waitcnt vmcnt(1)
	v_add_f32_e32 v28, v28, v36
	v_add_f32_e32 v29, v37, v29
	v_add_f32_e32 v30, v38, v30
	v_add_f32_e32 v31, v39, v31
	s_waitcnt vmcnt(0)
	v_add_f32_e32 v32, v32, v50
	v_add_f32_e32 v33, v51, v33
	v_add_f32_e32 v34, v52, v34
	s_waitcnt lgkmcnt(1)
	v_mfma_f32_32x32x16_f16 v[4:19], v[62:65], v[154:157], v[4:19]
	v_add_f32_e32 v35, v53, v35
	v_mul_f32_e32 v20, 0xbfb8aa3b, v20
	v_mul_f32_e32 v21, 0xbfb8aa3b, v21
	v_mul_f32_e32 v22, 0xbfb8aa3b, v22
	v_mul_f32_e32 v23, 0xbfb8aa3b, v23
	v_mul_f32_e32 v24, 0xbfb8aa3b, v24
	v_mul_f32_e32 v25, 0xbfb8aa3b, v25
	s_waitcnt lgkmcnt(0)
	v_mfma_f32_32x32x16_f16 v[4:19], v[66:69], v[158:161], v[4:19]
	v_mul_f32_e32 v26, 0xbfb8aa3b, v26
	v_mul_f32_e32 v27, 0xbfb8aa3b, v27
	v_mul_f32_e32 v28, 0xbfb8aa3b, v28
	v_mul_f32_e32 v29, 0xbfb8aa3b, v29
	v_mul_f32_e32 v30, 0xbfb8aa3b, v30
	v_mul_f32_e32 v31, 0xbfb8aa3b, v31
	v_mul_f32_e32 v32, 0xbfb8aa3b, v32
	v_mul_f32_e32 v33, 0xbfb8aa3b, v33
	v_mul_f32_e32 v34, 0xbfb8aa3b, v34
	v_mul_f32_e32 v35, 0xbfb8aa3b, v35
	v_exp_f32_e32 v20, v20
	v_exp_f32_e32 v21, v21
	v_exp_f32_e32 v22, v22
	v_exp_f32_e32 v23, v23
	v_exp_f32_e32 v24, v24
	v_exp_f32_e32 v25, v25
	v_exp_f32_e32 v26, v26
	v_exp_f32_e32 v27, v27
	v_exp_f32_e32 v28, v28
	v_exp_f32_e32 v29, v29
	v_exp_f32_e32 v30, v30
	v_exp_f32_e32 v31, v31
	v_exp_f32_e32 v32, v32
	v_exp_f32_e32 v33, v33
	v_exp_f32_e32 v34, v34
	v_exp_f32_e32 v35, v35
	v_add_f32_e32 v20, 1.0, v20
	v_add_f32_e32 v21, 1.0, v21
	v_add_f32_e32 v22, 1.0, v22
	v_add_f32_e32 v23, 1.0, v23
	v_add_f32_e32 v24, 1.0, v24
	v_add_f32_e32 v25, 1.0, v25
	v_add_f32_e32 v26, 1.0, v26
	v_add_f32_e32 v27, 1.0, v27
	v_add_f32_e32 v28, 1.0, v28
	v_add_f32_e32 v29, 1.0, v29
	v_add_f32_e32 v30, 1.0, v30
	v_add_f32_e32 v31, 1.0, v31
	v_add_f32_e32 v32, 1.0, v32
	v_add_f32_e32 v33, 1.0, v33
	v_add_f32_e32 v34, 1.0, v34
	v_add_f32_e32 v35, 1.0, v35
	v_rcp_f32_e32 v20, v20
	v_rcp_f32_e32 v21, v21
	v_rcp_f32_e32 v22, v22
	v_rcp_f32_e32 v23, v23
	v_rcp_f32_e32 v24, v24
	v_rcp_f32_e32 v25, v25
	v_rcp_f32_e32 v26, v26
	v_rcp_f32_e32 v27, v27
	v_rcp_f32_e32 v28, v28
	v_rcp_f32_e32 v29, v29
	v_rcp_f32_e32 v30, v30
	v_rcp_f32_e32 v31, v31
	v_rcp_f32_e32 v32, v32
	v_rcp_f32_e32 v33, v33
	v_rcp_f32_e32 v34, v34
	v_rcp_f32_e32 v35, v35
	v_cvt_pk_f16_f32 v198, v4, v5
	v_lshl_or_b32 v4, v222, 14, v1
	v_mov_b32_e32 v5, v2
	v_lshl_add_u64 v[216:217], s[28:29], 0, v[4:5]
	v_or_b32_e32 v4, 0x2000, v4
	v_lshrrev_b32_e32 v1, 1, v0
	v_lshl_add_u64 v[218:219], s[28:29], 0, v[4:5]
	v_and_b32_e32 v4, 16, v1
	v_mov_b32_e32 v36, 0x20000
	v_lshl_add_u64 v[4:5], s[36:37], 0, v[4:5]
	s_mov_b64 s[28:29], 0x80
	v_lshl_or_b32 v226, v96, 6, v36
	v_cvt_pk_f16_f32 v199, v6, v7
	v_cvt_pk_f16_f32 v200, v8, v9
	v_cvt_pk_f16_f32 v201, v10, v11
	v_cvt_pk_f16_f32 v202, v12, v13
	v_cvt_pk_f16_f32 v203, v14, v15
	v_cvt_pk_f16_f32 v204, v16, v17
	v_cvt_pk_f16_f32 v205, v18, v19
	v_cvt_pk_f16_f32 v229, v20, v21
	v_cvt_pk_f16_f32 v230, v22, v23
	v_cvt_pk_f16_f32 v232, v24, v25
	v_cvt_pk_f16_f32 v234, v26, v27
	v_cvt_pk_f16_f32 v228, v28, v29
	v_cvt_pk_f16_f32 v231, v30, v31
	v_cvt_pk_f16_f32 v233, v32, v33
	v_cvt_pk_f16_f32 v235, v34, v35
	v_lshl_add_u64 v[220:221], v[4:5], 0, s[28:29]
	s_mov_b64 s[36:37], 0
	s_branch .LBB1_6

.LBB1_59:
	s_setprio 0
	s_nop 10
	v_rcp_f32_e32 v8, v82
	v_cvt_f32_f16_sdwa v5, v229 dst_sel:DWORD dst_unused:UNUSED_PAD src0_sel:WORD_1
	v_cvt_f32_f16_e32 v4, v229
	v_cvt_f32_f16_sdwa v7, v230 dst_sel:DWORD dst_unused:UNUSED_PAD src0_sel:WORD_1
	v_cvt_f32_f16_e32 v6, v230
	v_cvt_f32_f16_sdwa v11, v232 dst_sel:DWORD dst_unused:UNUSED_PAD src0_sel:WORD_1
	v_cvt_f32_f16_e32 v10, v232
	v_cvt_f32_f16_sdwa v13, v234 dst_sel:DWORD dst_unused:UNUSED_PAD src0_sel:WORD_1
	v_cvt_f32_f16_e32 v12, v234
	v_pk_mul_f32 v[4:5], v[8:9], v[4:5] op_sel_hi:[0,1]
	v_pk_mul_f32 v[6:7], v[8:9], v[6:7] op_sel_hi:[0,1]
	v_pk_mul_f32 v[4:5], v[98:99], v[4:5]
	v_pk_mul_f32 v[6:7], v[100:101], v[6:7]
	v_cvt_pk_f16_f32 v4, v4, v5
	v_cvt_pk_f16_f32 v5, v6, v7
	v_pk_mul_f32 v[6:7], v[8:9], v[10:11] op_sel_hi:[0,1]
	v_pk_mul_f32 v[10:11], v[8:9], v[12:13] op_sel_hi:[0,1]
	v_pk_mul_f32 v[6:7], v[102:103], v[6:7]
	v_pk_mul_f32 v[10:11], v[104:105], v[10:11]
	v_cvt_pk_f16_f32 v6, v6, v7
	v_cvt_pk_f16_f32 v7, v10, v11
	v_cvt_f32_f16_sdwa v11, v228 dst_sel:DWORD dst_unused:UNUSED_PAD src0_sel:WORD_1
	v_cvt_f32_f16_e32 v10, v228
	ds_write_b128 v227, v[4:7]
	v_cvt_f32_f16_sdwa v7, v231 dst_sel:DWORD dst_unused:UNUSED_PAD src0_sel:WORD_1
	v_cvt_f32_f16_e32 v6, v231
	v_pk_mul_f32 v[4:5], v[8:9], v[10:11] op_sel_hi:[0,1]
	v_cvt_f32_f16_sdwa v11, v233 dst_sel:DWORD dst_unused:UNUSED_PAD src0_sel:WORD_1
	v_cvt_f32_f16_e32 v10, v233
	v_cvt_f32_f16_sdwa v13, v235 dst_sel:DWORD dst_unused:UNUSED_PAD src0_sel:WORD_1
	v_cvt_f32_f16_e32 v12, v235
	v_pk_mul_f32 v[6:7], v[8:9], v[6:7] op_sel_hi:[0,1]
	v_pk_mul_f32 v[4:5], v[4:5], v[106:107]
	v_pk_mul_f32 v[6:7], v[6:7], v[108:109]
	v_cvt_pk_f16_f32 v4, v4, v5
	v_cvt_pk_f16_f32 v5, v6, v7
	v_pk_mul_f32 v[6:7], v[8:9], v[10:11] op_sel_hi:[0,1]
	v_pk_mul_f32 v[8:9], v[8:9], v[12:13] op_sel_hi:[0,1]
	v_pk_mul_f32 v[6:7], v[6:7], v[110:111]
	v_pk_mul_f32 v[8:9], v[8:9], v[112:113]
	v_cvt_pk_f16_f32 v6, v6, v7
	v_cvt_pk_f16_f32 v7, v8, v9
	s_and_b64 vcc, exec, s[16:17]
	ds_write_b128 v227, v[4:7] offset:1024
	s_waitcnt vmcnt(0) lgkmcnt(2)
	s_barrier
	s_cbranch_vccnz .LBB1_5
	ds_read_b128 v[4:7], v206 offset:8192
	ds_read_b128 v[8:11], v206 offset:9216
	s_waitcnt lgkmcnt(1)
	v_mfma_f32_32x32x16_f16 v[114:129], v[4:7], v[130:133], 0
	ds_read_b128 v[4:7], v206 offset:16384
	ds_read_b128 v[12:15], v206 offset:17408
	s_waitcnt lgkmcnt(1)
	v_mfma_f32_32x32x16_f16 v[98:113], v[130:133], v[4:7], 0
	v_mfma_f32_32x32x16_f16 v[114:129], v[8:11], v[134:137], v[114:129]
	ds_read_b128 v[4:7], v206 offset:10240
	ds_read_b128 v[8:11], v206 offset:11264
	s_waitcnt lgkmcnt(2)
	v_mfma_f32_32x32x16_f16 v[98:113], v[134:137], v[12:15], v[98:113]
	s_waitcnt lgkmcnt(1)
	v_mfma_f32_32x32x16_f16 v[114:129], v[4:7], v[138:141], v[114:129]
	ds_read_b128 v[4:7], v206 offset:18432
	ds_read_b128 v[12:15], v206 offset:19456
	s_waitcnt lgkmcnt(1)
	v_mfma_f32_32x32x16_f16 v[98:113], v[138:141], v[4:7], v[98:113]
	v_mfma_f32_32x32x16_f16 v[114:129], v[8:11], v[142:145], v[114:129]
	ds_read_b128 v[4:7], v206 offset:12288
	ds_read_b128 v[8:11], v206 offset:13312
	s_waitcnt lgkmcnt(2)
	v_mfma_f32_32x32x16_f16 v[98:113], v[142:145], v[12:15], v[98:113]
	s_waitcnt lgkmcnt(1)
	v_mfma_f32_32x32x16_f16 v[114:129], v[4:7], v[146:149], v[114:129]
	ds_read_b128 v[4:7], v206 offset:20480
	ds_read_b128 v[12:15], v206 offset:21504
	s_waitcnt lgkmcnt(1)
	v_mfma_f32_32x32x16_f16 v[98:113], v[146:149], v[4:7], v[98:113]
	v_mfma_f32_32x32x16_f16 v[114:129], v[8:11], v[150:153], v[114:129]
	ds_read_b128 v[4:7], v206 offset:14336
	ds_read_b128 v[8:11], v206 offset:15360
	s_waitcnt lgkmcnt(2)
	v_mfma_f32_32x32x16_f16 v[98:113], v[150:153], v[12:15], v[98:113]
	s_waitcnt lgkmcnt(1)
	v_mfma_f32_32x32x16_f16 v[114:129], v[4:7], v[154:157], v[114:129]
	ds_read_b128 v[4:7], v206 offset:22528
	ds_read_b128 v[12:15], v206 offset:23552
	s_waitcnt lgkmcnt(1)
	v_mfma_f32_32x32x16_f16 v[98:113], v[154:157], v[4:7], v[98:113]
	v_mfma_f32_32x32x16_f16 v[114:129], v[8:11], v[158:161], v[114:129]
	ds_read_b128 v[4:7], v206 offset:24576
	ds_read_b128 v[8:11], v206 offset:25600
	s_waitcnt lgkmcnt(1)
	v_mfma_f32_32x32x16_f16 v[82:97], v[4:7], v[130:133], 0
	global_load_dwordx4 v[4:7], v[220:221], off
	s_nop 6
	v_cvt_pk_f16_f32 v121, v120, v121
	v_cvt_pk_f16_f32 v120, v118, v119
	v_cvt_pk_f16_f32 v119, v116, v117
	v_cvt_pk_f16_f32 v118, v114, v115
	v_cvt_pk_f16_f32 v117, v128, v129
	v_cvt_pk_f16_f32 v116, v126, v127
	s_waitcnt lgkmcnt(0)
	v_mfma_f32_32x32x16_f16 v[82:97], v[8:11], v[134:137], v[82:97]
	v_cvt_pk_f16_f32 v115, v124, v125
	v_cvt_pk_f16_f32 v114, v122, v123
	v_mfma_f32_32x32x16_f16 v[98:113], v[158:161], v[12:15], v[98:113]
	ds_read_b128 v[8:11], v206 offset:26624
	ds_read_b128 v[12:15], v206 offset:27648
	ds_read_b128 v[196:199], v206 offset:28672
	ds_write_b128 v209, v[114:117] offset:33792
	global_load_dwordx4 v[114:117], v[220:221], off offset:96
	ds_write_b128 v209, v[118:121] offset:32768
	ds_read_b128 v[118:121], v206 offset:29696
	s_nop 4
	v_cvt_pk_f16_f32 v105, v104, v105
	s_waitcnt lgkmcnt(5)
	v_mfma_f32_32x32x16_f16 v[82:97], v[8:11], v[138:141], v[82:97]
	global_load_dwordx4 v[8:11], v[220:221], off offset:32
	v_cvt_pk_f16_f32 v104, v102, v103
	v_cvt_pk_f16_f32 v103, v100, v101
	v_cvt_pk_f16_f32 v102, v98, v99
	ds_read_b128 v[98:101], v206 offset:30720
	ds_write_b128 v209, v[102:105] offset:49152
	v_cvt_pk_f16_f32 v103, v108, v109
	s_waitcnt lgkmcnt(6)
	v_mfma_f32_32x32x16_f16 v[82:97], v[12:15], v[142:145], v[82:97]
	global_load_dwordx4 v[12:15], v[220:221], off offset:64
	v_cvt_pk_f16_f32 v102, v106, v107
	ds_read_b128 v[106:109], v206 offset:31744
	v_cvt_pk_f16_f32 v105, v112, v113
	v_cvt_pk_f16_f32 v104, v110, v111
	ds_write_b128 v209, v[102:105] offset:50176
	s_waitcnt lgkmcnt(7)
	v_mfma_f32_32x32x16_f16 v[82:97], v[196:199], v[146:149], v[82:97]
	s_waitcnt lgkmcnt(4)
	v_mfma_f32_32x32x16_f16 v[82:97], v[118:121], v[150:153], v[82:97]
	s_waitcnt lgkmcnt(3)
	v_mfma_f32_32x32x16_f16 v[82:97], v[98:101], v[154:157], v[82:97]
	ds_read_b128 v[98:101], v206
	ds_read_b128 v[118:121], v206 offset:1024
	ds_read_b128 v[122:125], v206 offset:2048
	ds_read_b128 v[126:129], v206 offset:3072
	ds_read_b128 v[196:199], v206 offset:4096
	ds_read_b128 v[200:203], v206 offset:5120
	ds_read_b128 v[230:233], v206 offset:6144
	ds_read_b128 v[236:239], v206 offset:7168
	s_waitcnt lgkmcnt(8)
	s_barrier
	v_mfma_f32_32x32x16_f16 v[82:97], v[106:109], v[158:161], v[82:97]
	s_waitcnt lgkmcnt(7)
	v_mfma_f32_32x32x16_f16 v[98:113], v[98:101], v[130:133], 0
	s_waitcnt vmcnt(3)
	s_nop 9
	v_add_f32_e32 v1, v82, v4
	s_waitcnt lgkmcnt(6)
	v_mfma_f32_32x32x16_f16 v[98:113], v[118:121], v[134:137], v[98:113]
	v_add_f32_e32 v3, v5, v83
	v_add_f32_e32 v4, v6, v84
	v_add_f32_e32 v5, v7, v85
	v_mul_f32_e32 v1, 0xbfb8aa3b, v1
	v_mul_f32_e32 v3, 0xbfb8aa3b, v3
	v_mul_f32_e32 v4, 0xbfb8aa3b, v4
	v_mul_f32_e32 v5, 0xbfb8aa3b, v5
	s_waitcnt lgkmcnt(5)
	v_mfma_f32_32x32x16_f16 v[98:113], v[122:125], v[138:141], v[98:113]
	v_exp_f32_e32 v1, v1
	v_exp_f32_e32 v3, v3
	v_exp_f32_e32 v4, v4
	v_exp_f32_e32 v5, v5
	v_add_f32_e32 v1, 1.0, v1
	v_add_f32_e32 v3, 1.0, v3
	v_add_f32_e32 v4, 1.0, v4
	s_waitcnt lgkmcnt(4)
	v_mfma_f32_32x32x16_f16 v[98:113], v[126:129], v[142:145], v[98:113]
	v_add_f32_e32 v5, 1.0, v5
	s_waitcnt vmcnt(2)
	v_add_f32_e32 v16, v116, v96
	v_add_f32_e32 v17, v117, v97
	v_mul_f32_e32 v16, 0xbfb8aa3b, v16
	v_mul_f32_e32 v17, 0xbfb8aa3b, v17
	v_exp_f32_e32 v16, v16
	v_exp_f32_e32 v17, v17
	s_waitcnt lgkmcnt(3)
	v_mfma_f32_32x32x16_f16 v[98:113], v[196:199], v[146:149], v[98:113]
	s_waitcnt vmcnt(1)
	v_add_f32_e32 v6, v86, v8
	v_add_f32_e32 v7, v9, v87
	v_add_f32_e32 v8, v10, v88
	v_add_f32_e32 v9, v11, v89
	v_mul_f32_e32 v6, 0xbfb8aa3b, v6
	v_mul_f32_e32 v7, 0xbfb8aa3b, v7
	v_mul_f32_e32 v8, 0xbfb8aa3b, v8
	s_waitcnt lgkmcnt(2)
	v_mfma_f32_32x32x16_f16 v[98:113], v[200:203], v[150:153], v[98:113]
	s_waitcnt vmcnt(0)
	v_add_f32_e32 v10, v90, v12
	v_add_f32_e32 v11, v13, v91
	v_add_f32_e32 v12, v14, v92
	v_add_f32_e32 v13, v15, v93
	v_add_f32_e32 v14, v94, v114
	v_add_f32_e32 v15, v115, v95
	v_mul_f32_e32 v9, 0xbfb8aa3b, v9
	s_waitcnt lgkmcnt(1)
	v_mfma_f32_32x32x16_f16 v[98:113], v[230:233], v[154:157], v[98:113]
	v_mul_f32_e32 v10, 0xbfb8aa3b, v10
	v_mul_f32_e32 v11, 0xbfb8aa3b, v11
	v_mul_f32_e32 v12, 0xbfb8aa3b, v12
	v_mul_f32_e32 v13, 0xbfb8aa3b, v13
	v_mul_f32_e32 v14, 0xbfb8aa3b, v14
	v_mul_f32_e32 v15, 0xbfb8aa3b, v15
	v_exp_f32_e32 v6, v6
	v_exp_f32_e32 v7, v7
	v_exp_f32_e32 v8, v8
	v_exp_f32_e32 v9, v9
	v_exp_f32_e32 v10, v10
	v_exp_f32_e32 v11, v11
	v_exp_f32_e32 v12, v12
	v_exp_f32_e32 v13, v13
	v_exp_f32_e32 v14, v14
	v_exp_f32_e32 v15, v15
	s_waitcnt lgkmcnt(0)
	v_mfma_f32_32x32x16_f16 v[98:113], v[236:239], v[158:161], v[98:113]
	v_add_f32_e32 v6, 1.0, v6
	v_add_f32_e32 v7, 1.0, v7
	v_add_f32_e32 v8, 1.0, v8
	v_add_f32_e32 v9, 1.0, v9
	v_add_f32_e32 v10, 1.0, v10
	v_add_f32_e32 v11, 1.0, v11
	v_add_f32_e32 v12, 1.0, v12
	v_add_f32_e32 v13, 1.0, v13
	v_add_f32_e32 v14, 1.0, v14
	v_add_f32_e32 v15, 1.0, v15
	v_add_f32_e32 v16, 1.0, v16
	v_add_f32_e32 v17, 1.0, v17
	v_rcp_f32_e32 v1, v1
	v_rcp_f32_e32 v3, v3
	v_rcp_f32_e32 v4, v4
	v_rcp_f32_e32 v5, v5
	v_rcp_f32_e32 v6, v6
	v_rcp_f32_e32 v7, v7
	v_rcp_f32_e32 v8, v8
	v_rcp_f32_e32 v9, v9
	v_rcp_f32_e32 v10, v10
	v_rcp_f32_e32 v11, v11
	v_rcp_f32_e32 v12, v12
	v_rcp_f32_e32 v13, v13
	v_rcp_f32_e32 v14, v14
	v_rcp_f32_e32 v15, v15
	v_rcp_f32_e32 v16, v16
	v_rcp_f32_e32 v17, v17
	v_cvt_pk_f16_f32 v228, v10, v11
	v_cvt_pk_f16_f32 v231, v12, v13
	v_cvt_pk_f16_f32 v233, v14, v15
	v_cvt_pk_f16_f32 v235, v16, v17
	v_cvt_pk_f16_f32 v229, v1, v3
	v_cvt_pk_f16_f32 v230, v4, v5
	v_cvt_pk_f16_f32 v232, v6, v7
	v_cvt_pk_f16_f32 v234, v8, v9
	v_cvt_pk_f16_f32 v202, v106, v107
	v_cvt_pk_f16_f32 v203, v108, v109
	v_cvt_pk_f16_f32 v204, v110, v111
	v_cvt_pk_f16_f32 v205, v112, v113
	v_cvt_pk_f16_f32 v198, v98, v99
	v_cvt_pk_f16_f32 v199, v100, v101
	v_cvt_pk_f16_f32 v200, v102, v103
	v_cvt_pk_f16_f32 v201, v104, v105
	s_branch .LBB1_5
